# c41: c40 + attention bias-table fill (both layers) issues its five table loads before a single wait instead of load-wait per iteration
# speedup vs baseline: 1.0102x; 1.0003x over previous
; #define LAS __attribute__((address_space(3)))
; __device__ __forceinline__ void fill_bias_tables(LAS unsigned char* lds, int tid, const float* table, bool dilated) {
;     for (int idx = tid; idx < 12 * BT_FLOATS; idx += NTHREADS) { const int h = idx / BT_FLOATS, j = idx - h * BT_FLOATS, o = 159 - j;
;         const int dil = dilated ? (1 << (2 * (h >> 2))) : 1, maxd = dilated ? 128 : 127; float val = -1e30f;
;         if (o >= 0 && o <= maxd) val = table[t5_bucket(o * dil) * 12 + h] * LOG2E;
;         ((LAS float*)(lds + B_OFF))[idx] = val; }
; }
.LBB0_361:
	v_mov_b32_e32 v190, 0
	v_mul_u32_u24_e32 v2, 0xaaab, v6
	v_lshrrev_b32_e32 v2, 23, v2
	v_mul_i32_i24_e32 v8, 0xffffff40, v2
	v_add3_u32 v7, v8, v6, s4
	v_cmp_lt_u32_e32 vcc, s5, v7
	v_mov_b32_e32 v7, 0xf149f2ca
	s_and_saveexec_b64 s[12:13], vcc
	s_cbranch_execz .Lbfa_t0
	v_sub_u32_e32 v7, v4, v8
	v_cmp_lt_u32_e32 vcc, 15, v7
	s_and_saveexec_b64 s[14:15], vcc
	s_cbranch_execz .Lbfa_l0
	v_cvt_f32_u32_e32 v7, v7
	v_mul_f32_e32 v7, 0x3d800000, v7
	v_cmp_gt_f32_e32 vcc, s6, v7
	s_nop 1
	v_cndmask_b32_e64 v8, 0, 32, vcc
	v_ldexp_f32 v7, v7, v8
	v_log_f32_e32 v7, v7
	v_cndmask_b32_e32 v8, 0, v5, vcc
	v_mul_f32_e32 v9, 0x3f317217, v7
	v_fma_f32 v9, v7, s7, -v9
	v_fmac_f32_e32 v9, 0x3377d1cf, v7
	v_fmac_f32_e32 v9, 0x3f317217, v7
	v_cmp_lt_f32_e64 vcc, |v7|, s16
	s_nop 1
	v_cndmask_b32_e32 v7, v7, v9, vcc
	v_sub_f32_e32 v7, v7, v8
	v_div_scale_f32 v8, s[22:23], s17, s17, v7
	v_rcp_f32_e32 v9, v8
	v_div_scale_f32 v10, vcc, v7, s17, v7
	v_fma_f32 v11, -v8, v9, 1.0
	v_fmac_f32_e32 v9, v11, v9
	v_mul_f32_e32 v11, v10, v9
	v_fma_f32 v12, -v8, v11, v10
	v_fmac_f32_e32 v11, v12, v9
	v_fma_f32 v8, -v8, v11, v10
	v_div_fmas_f32 v8, v8, v9, v11
	v_div_fixup_f32 v7, v8, s17, v7
	v_mul_f32_e32 v7, 0x41800000, v7
	v_cvt_i32_f32_e32 v7, v7
	v_min_i32_e32 v7, 15, v7
	v_add_u32_e32 v7, 16, v7
	s_branch .Lbfa_l0
.Lbfa_l0:
	s_or_b64 exec, exec, s[14:15]
	v_mad_u64_u32 v[8:9], s[14:15], v7, 12, v[2:3]
	v_ashrrev_i32_e32 v9, 31, v8
	v_lshl_add_u64 v[8:9], v[8:9], 2, s[20:21]
	global_load_dword v185, v[8:9], off
	v_mov_b32_e32 v190, 1
.Lbfa_t0:
	s_or_b64 exec, exec, s[12:13]
	v_add_u32_e32 v6, 0x200, v6
	v_add_u32_e32 v4, 0xfffffe00, v4
	v_mov_b32_e32 v191, 0
	v_mul_u32_u24_e32 v2, 0xaaab, v6
	v_lshrrev_b32_e32 v2, 23, v2
	v_mul_i32_i24_e32 v8, 0xffffff40, v2
	v_add3_u32 v7, v8, v6, s4
	v_cmp_lt_u32_e32 vcc, s5, v7
	v_mov_b32_e32 v7, 0xf149f2ca
	s_and_saveexec_b64 s[12:13], vcc
	s_cbranch_execz .Lbfa_t1
	v_sub_u32_e32 v7, v4, v8
	v_cmp_lt_u32_e32 vcc, 15, v7
	s_and_saveexec_b64 s[14:15], vcc
	s_cbranch_execz .Lbfa_l1
	v_cvt_f32_u32_e32 v7, v7
	v_mul_f32_e32 v7, 0x3d800000, v7
	v_cmp_gt_f32_e32 vcc, s6, v7
	s_nop 1
	v_cndmask_b32_e64 v8, 0, 32, vcc
	v_ldexp_f32 v7, v7, v8
	v_log_f32_e32 v7, v7
	v_cndmask_b32_e32 v8, 0, v5, vcc
	v_mul_f32_e32 v9, 0x3f317217, v7
	v_fma_f32 v9, v7, s7, -v9
	v_fmac_f32_e32 v9, 0x3377d1cf, v7
	v_fmac_f32_e32 v9, 0x3f317217, v7
	v_cmp_lt_f32_e64 vcc, |v7|, s16
	s_nop 1
	v_cndmask_b32_e32 v7, v7, v9, vcc
	v_sub_f32_e32 v7, v7, v8
	v_div_scale_f32 v8, s[22:23], s17, s17, v7
	v_rcp_f32_e32 v9, v8
	v_div_scale_f32 v10, vcc, v7, s17, v7
	v_fma_f32 v11, -v8, v9, 1.0
	v_fmac_f32_e32 v9, v11, v9
	v_mul_f32_e32 v11, v10, v9
	v_fma_f32 v12, -v8, v11, v10
	v_fmac_f32_e32 v11, v12, v9
	v_fma_f32 v8, -v8, v11, v10
	v_div_fmas_f32 v8, v8, v9, v11
	v_div_fixup_f32 v7, v8, s17, v7
	v_mul_f32_e32 v7, 0x41800000, v7
	v_cvt_i32_f32_e32 v7, v7
	v_min_i32_e32 v7, 15, v7
	v_add_u32_e32 v7, 16, v7
	s_branch .Lbfa_l1
.Lbfa_l1:
	s_or_b64 exec, exec, s[14:15]
	v_mad_u64_u32 v[8:9], s[14:15], v7, 12, v[2:3]
	v_ashrrev_i32_e32 v9, 31, v8
	v_lshl_add_u64 v[8:9], v[8:9], 2, s[20:21]
	global_load_dword v186, v[8:9], off
	v_mov_b32_e32 v191, 1
.Lbfa_t1:
	s_or_b64 exec, exec, s[12:13]
	v_add_u32_e32 v6, 0x200, v6
	v_add_u32_e32 v4, 0xfffffe00, v4
	v_mov_b32_e32 v192, 0
	v_mul_u32_u24_e32 v2, 0xaaab, v6
	v_lshrrev_b32_e32 v2, 23, v2
	v_mul_i32_i24_e32 v8, 0xffffff40, v2
	v_add3_u32 v7, v8, v6, s4
	v_cmp_lt_u32_e32 vcc, s5, v7
	v_mov_b32_e32 v7, 0xf149f2ca
	s_and_saveexec_b64 s[12:13], vcc
	s_cbranch_execz .Lbfa_t2
	v_sub_u32_e32 v7, v4, v8
	v_cmp_lt_u32_e32 vcc, 15, v7
	s_and_saveexec_b64 s[14:15], vcc
	s_cbranch_execz .Lbfa_l2
	v_cvt_f32_u32_e32 v7, v7
	v_mul_f32_e32 v7, 0x3d800000, v7
	v_cmp_gt_f32_e32 vcc, s6, v7
	s_nop 1
	v_cndmask_b32_e64 v8, 0, 32, vcc
	v_ldexp_f32 v7, v7, v8
	v_log_f32_e32 v7, v7
	v_cndmask_b32_e32 v8, 0, v5, vcc
	v_mul_f32_e32 v9, 0x3f317217, v7
	v_fma_f32 v9, v7, s7, -v9
	v_fmac_f32_e32 v9, 0x3377d1cf, v7
	v_fmac_f32_e32 v9, 0x3f317217, v7
	v_cmp_lt_f32_e64 vcc, |v7|, s16
	s_nop 1
	v_cndmask_b32_e32 v7, v7, v9, vcc
	v_sub_f32_e32 v7, v7, v8
	v_div_scale_f32 v8, s[22:23], s17, s17, v7
	v_rcp_f32_e32 v9, v8
	v_div_scale_f32 v10, vcc, v7, s17, v7
	v_fma_f32 v11, -v8, v9, 1.0
	v_fmac_f32_e32 v9, v11, v9
	v_mul_f32_e32 v11, v10, v9
	v_fma_f32 v12, -v8, v11, v10
	v_fmac_f32_e32 v11, v12, v9
	v_fma_f32 v8, -v8, v11, v10
	v_div_fmas_f32 v8, v8, v9, v11
	v_div_fixup_f32 v7, v8, s17, v7
	v_mul_f32_e32 v7, 0x41800000, v7
	v_cvt_i32_f32_e32 v7, v7
	v_min_i32_e32 v7, 15, v7
	v_add_u32_e32 v7, 16, v7
	s_branch .Lbfa_l2
; #define LAS __attribute__((address_space(3)))
; __device__ __forceinline__ void fill_bias_tables(LAS unsigned char* lds, int tid, const float* table, bool dilated) {
;     for (int idx = tid; idx < 12 * BT_FLOATS; idx += NTHREADS) { const int h = idx / BT_FLOATS, j = idx - h * BT_FLOATS, o = 159 - j;
;         const int dil = dilated ? (1 << (2 * (h >> 2))) : 1, maxd = dilated ? 128 : 127; float val = -1e30f;
;         if (o >= 0 && o <= maxd) val = table[t5_bucket(o * dil) * 12 + h] * LOG2E;
;         ((LAS float*)(lds + B_OFF))[idx] = val; }
; }
.Lbfa_l2:
	s_or_b64 exec, exec, s[14:15]
	v_mad_u64_u32 v[8:9], s[14:15], v7, 12, v[2:3]
	v_ashrrev_i32_e32 v9, 31, v8
	v_lshl_add_u64 v[8:9], v[8:9], 2, s[20:21]
	global_load_dword v187, v[8:9], off
	v_mov_b32_e32 v192, 1
.Lbfa_t2:
	s_or_b64 exec, exec, s[12:13]
	v_add_u32_e32 v6, 0x200, v6
	v_add_u32_e32 v4, 0xfffffe00, v4
	v_mov_b32_e32 v193, 0
	v_mul_u32_u24_e32 v2, 0xaaab, v6
	v_lshrrev_b32_e32 v2, 23, v2
	v_mul_i32_i24_e32 v8, 0xffffff40, v2
	v_add3_u32 v7, v8, v6, s4
	v_cmp_lt_u32_e32 vcc, s5, v7
	v_mov_b32_e32 v7, 0xf149f2ca
	s_and_saveexec_b64 s[12:13], vcc
	s_cbranch_execz .Lbfa_t3
	v_sub_u32_e32 v7, v4, v8
	v_cmp_lt_u32_e32 vcc, 15, v7
	s_and_saveexec_b64 s[14:15], vcc
	s_cbranch_execz .Lbfa_l3
	v_cvt_f32_u32_e32 v7, v7
	v_mul_f32_e32 v7, 0x3d800000, v7
	v_cmp_gt_f32_e32 vcc, s6, v7
	s_nop 1
	v_cndmask_b32_e64 v8, 0, 32, vcc
	v_ldexp_f32 v7, v7, v8
	v_log_f32_e32 v7, v7
	v_cndmask_b32_e32 v8, 0, v5, vcc
	v_mul_f32_e32 v9, 0x3f317217, v7
	v_fma_f32 v9, v7, s7, -v9
	v_fmac_f32_e32 v9, 0x3377d1cf, v7
	v_fmac_f32_e32 v9, 0x3f317217, v7
	v_cmp_lt_f32_e64 vcc, |v7|, s16
	s_nop 1
	v_cndmask_b32_e32 v7, v7, v9, vcc
	v_sub_f32_e32 v7, v7, v8
	v_div_scale_f32 v8, s[22:23], s17, s17, v7
	v_rcp_f32_e32 v9, v8
	v_div_scale_f32 v10, vcc, v7, s17, v7
	v_fma_f32 v11, -v8, v9, 1.0
	v_fmac_f32_e32 v9, v11, v9
	v_mul_f32_e32 v11, v10, v9
	v_fma_f32 v12, -v8, v11, v10
	v_fmac_f32_e32 v11, v12, v9
	v_fma_f32 v8, -v8, v11, v10
	v_div_fmas_f32 v8, v8, v9, v11
	v_div_fixup_f32 v7, v8, s17, v7
	v_mul_f32_e32 v7, 0x41800000, v7
	v_cvt_i32_f32_e32 v7, v7
	v_min_i32_e32 v7, 15, v7
	v_add_u32_e32 v7, 16, v7
	s_branch .Lbfa_l3
.Lbfa_l3:
	s_or_b64 exec, exec, s[14:15]
	v_mad_u64_u32 v[8:9], s[14:15], v7, 12, v[2:3]
	v_ashrrev_i32_e32 v9, 31, v8
	v_lshl_add_u64 v[8:9], v[8:9], 2, s[20:21]
	global_load_dword v188, v[8:9], off
	v_mov_b32_e32 v193, 1
.Lbfa_t3:
	s_or_b64 exec, exec, s[12:13]
	v_add_u32_e32 v6, 0x200, v6
	v_add_u32_e32 v4, 0xfffffe00, v4
	v_cmp_gt_u32_e32 vcc, 0x900, v6
	s_and_saveexec_b64 s[8:9], vcc
	s_cbranch_execz .Lbfa_skip4
	v_mov_b32_e32 v194, 0
	v_mul_u32_u24_e32 v2, 0xaaab, v6
	v_lshrrev_b32_e32 v2, 23, v2
	v_mul_i32_i24_e32 v8, 0xffffff40, v2
	v_add3_u32 v7, v8, v6, s4
	v_cmp_lt_u32_e32 vcc, s5, v7
	v_mov_b32_e32 v7, 0xf149f2ca
	s_and_saveexec_b64 s[12:13], vcc
	s_cbranch_execz .Lbfa_t4
	v_sub_u32_e32 v7, v4, v8
	v_cmp_lt_u32_e32 vcc, 15, v7
	s_and_saveexec_b64 s[14:15], vcc
	s_cbranch_execz .Lbfa_l4
	v_cvt_f32_u32_e32 v7, v7
	v_mul_f32_e32 v7, 0x3d800000, v7
	v_cmp_gt_f32_e32 vcc, s6, v7
	s_nop 1
	v_cndmask_b32_e64 v8, 0, 32, vcc
	v_ldexp_f32 v7, v7, v8
	v_log_f32_e32 v7, v7
	v_cndmask_b32_e32 v8, 0, v5, vcc
	v_mul_f32_e32 v9, 0x3f317217, v7
	v_fma_f32 v9, v7, s7, -v9
	v_fmac_f32_e32 v9, 0x3377d1cf, v7
	v_fmac_f32_e32 v9, 0x3f317217, v7
	v_cmp_lt_f32_e64 vcc, |v7|, s16
	s_nop 1
	v_cndmask_b32_e32 v7, v7, v9, vcc
	v_sub_f32_e32 v7, v7, v8
	v_div_scale_f32 v8, s[22:23], s17, s17, v7
	v_rcp_f32_e32 v9, v8
	v_div_scale_f32 v10, vcc, v7, s17, v7
	v_fma_f32 v11, -v8, v9, 1.0
	v_fmac_f32_e32 v9, v11, v9
	v_mul_f32_e32 v11, v10, v9
	v_fma_f32 v12, -v8, v11, v10
	v_fmac_f32_e32 v11, v12, v9
	v_fma_f32 v8, -v8, v11, v10
	v_div_fmas_f32 v8, v8, v9, v11
	v_div_fixup_f32 v7, v8, s17, v7
	v_mul_f32_e32 v7, 0x41800000, v7
	v_cvt_i32_f32_e32 v7, v7
	v_min_i32_e32 v7, 15, v7
	v_add_u32_e32 v7, 16, v7
	s_branch .Lbfa_l4
.Lbfa_l4:
	s_or_b64 exec, exec, s[14:15]
	v_mad_u64_u32 v[8:9], s[14:15], v7, 12, v[2:3]
	v_ashrrev_i32_e32 v9, 31, v8
	v_lshl_add_u64 v[8:9], v[8:9], 2, s[20:21]
	global_load_dword v189, v[8:9], off
	v_mov_b32_e32 v194, 1
.Lbfa_t4:
	s_or_b64 exec, exec, s[12:13]
	v_add_u32_e32 v6, 0x200, v6
	v_add_u32_e32 v4, 0xfffffe00, v4
.Lbfa_skip4:
	s_or_b64 exec, exec, s[8:9]
	s_waitcnt vmcnt(0)
	v_mov_b32_e32 v195, 0xf149f2ca
	v_mul_f32_e32 v7, 0x3fb8aa3b, v185
	v_cmp_eq_u32_e32 vcc, 1, v190
	s_nop 1
	v_cndmask_b32_e32 v7, v195, v7, vcc
	ds_write_b32 v3, v7
	v_add_u32_e32 v3, 0x800, v3
	v_mul_f32_e32 v7, 0x3fb8aa3b, v186
	v_cmp_eq_u32_e32 vcc, 1, v191
	s_nop 1
	v_cndmask_b32_e32 v7, v195, v7, vcc
	ds_write_b32 v3, v7
	v_add_u32_e32 v3, 0x800, v3
	v_mul_f32_e32 v7, 0x3fb8aa3b, v187
	v_cmp_eq_u32_e32 vcc, 1, v192
	s_nop 1
	v_cndmask_b32_e32 v7, v195, v7, vcc
	ds_write_b32 v3, v7
	v_add_u32_e32 v3, 0x800, v3
	v_mul_f32_e32 v7, 0x3fb8aa3b, v188
	v_cmp_eq_u32_e32 vcc, 1, v193
	s_nop 1
	v_cndmask_b32_e32 v7, v195, v7, vcc
	ds_write_b32 v3, v7
	v_add_u32_e32 v3, 0x800, v3
	v_cmp_gt_u32_e32 vcc, 0x100, v0
	s_and_saveexec_b64 s[8:9], vcc
	s_cbranch_execz .LBB0_364
	v_mul_f32_e32 v7, 0x3fb8aa3b, v189
	v_cmp_eq_u32_e32 vcc, 1, v194
	s_nop 1
	v_cndmask_b32_e32 v7, v195, v7, vcc
	ds_write_b32 v3, v7
	v_add_u32_e32 v3, 0x800, v3

; #define LAS __attribute__((address_space(3)))
; __device__ __forceinline__ void fill_bias_tables(LAS unsigned char* lds, int tid, const float* table, bool dilated) {
;     for (int idx = tid; idx < 12 * BT_FLOATS; idx += NTHREADS) { const int h = idx / BT_FLOATS, j = idx - h * BT_FLOATS, o = 159 - j;
;         const int dil = dilated ? (1 << (2 * (h >> 2))) : 1, maxd = dilated ? 128 : 127; float val = -1e30f;
;         if (o >= 0 && o <= maxd) val = table[t5_bucket(o * dil) * 12 + h] * LOG2E;
;         ((LAS float*)(lds + B_OFF))[idx] = val; }
; }
.LBB0_930:
	v_mov_b32_e32 v190, 0
	v_mul_u32_u24_e32 v2, 0xaaab, v6
	v_lshrrev_b32_e32 v2, 23, v2
	v_mul_i32_i24_e32 v8, 0xffffff40, v2
	v_add3_u32 v7, v8, v6, s3
	v_cmp_lt_u32_e32 vcc, s4, v7
	v_mov_b32_e32 v7, 0xf149f2ca
	s_and_saveexec_b64 s[10:11], vcc
	s_cbranch_execz .Lbfb_t0
	v_sub_u32_e32 v7, v4, v8
	v_lshrrev_b32_e32 v8, 1, v2
	v_and_b32_e32 v8, 14, v8
	v_lshlrev_b32_e32 v7, v8, v7
	v_cmp_lt_u32_e32 vcc, 15, v7
	s_and_saveexec_b64 s[12:13], vcc
	s_cbranch_execz .Lbfb_l0
	v_cvt_f32_u32_e32 v7, v7
	v_mul_f32_e32 v7, 0x3d800000, v7
	v_cmp_gt_f32_e32 vcc, s5, v7
	s_nop 1
	v_cndmask_b32_e64 v8, 0, 32, vcc
	v_ldexp_f32 v7, v7, v8
	v_log_f32_e32 v7, v7
	v_cndmask_b32_e32 v8, 0, v5, vcc
	v_mul_f32_e32 v9, 0x3f317217, v7
	v_fma_f32 v9, v7, s6, -v9
	v_fmac_f32_e32 v9, 0x3377d1cf, v7
	v_fmac_f32_e32 v9, 0x3f317217, v7
	v_cmp_lt_f32_e64 vcc, |v7|, s7
	s_nop 1
	v_cndmask_b32_e32 v7, v7, v9, vcc
	v_sub_f32_e32 v7, v7, v8
	v_div_scale_f32 v8, s[18:19], s16, s16, v7
	v_rcp_f32_e32 v9, v8
	v_div_scale_f32 v10, vcc, v7, s16, v7
	v_fma_f32 v11, -v8, v9, 1.0
	v_fmac_f32_e32 v9, v11, v9
	v_mul_f32_e32 v11, v10, v9
	v_fma_f32 v12, -v8, v11, v10
	v_fmac_f32_e32 v11, v12, v9
	v_fma_f32 v8, -v8, v11, v10
	v_div_fmas_f32 v8, v8, v9, v11
	v_div_fixup_f32 v7, v8, s16, v7
	v_mul_f32_e32 v7, 0x41800000, v7
	v_cvt_i32_f32_e32 v7, v7
	v_min_i32_e32 v7, 15, v7
	v_add_u32_e32 v7, 16, v7
	s_branch .Lbfb_l0
.Lbfb_l0:
	s_or_b64 exec, exec, s[12:13]
	v_mad_u64_u32 v[8:9], s[12:13], v7, 12, v[2:3]
	v_ashrrev_i32_e32 v9, 31, v8
	v_lshl_add_u64 v[8:9], v[8:9], 2, s[20:21]
	global_load_dword v185, v[8:9], off
	v_mov_b32_e32 v190, 1
.Lbfb_t0:
	s_or_b64 exec, exec, s[10:11]
	v_add_u32_e32 v6, 0x200, v6
	v_add_u32_e32 v4, 0xfffffe00, v4
	v_mov_b32_e32 v191, 0
	v_mul_u32_u24_e32 v2, 0xaaab, v6
	v_lshrrev_b32_e32 v2, 23, v2
	v_mul_i32_i24_e32 v8, 0xffffff40, v2
	v_add3_u32 v7, v8, v6, s3
	v_cmp_lt_u32_e32 vcc, s4, v7
	v_mov_b32_e32 v7, 0xf149f2ca
	s_and_saveexec_b64 s[10:11], vcc
	s_cbranch_execz .Lbfb_t1
	v_sub_u32_e32 v7, v4, v8
	v_lshrrev_b32_e32 v8, 1, v2
	v_and_b32_e32 v8, 14, v8
	v_lshlrev_b32_e32 v7, v8, v7
	v_cmp_lt_u32_e32 vcc, 15, v7
	s_and_saveexec_b64 s[12:13], vcc
	s_cbranch_execz .Lbfb_l1
	v_cvt_f32_u32_e32 v7, v7
	v_mul_f32_e32 v7, 0x3d800000, v7
	v_cmp_gt_f32_e32 vcc, s5, v7
	s_nop 1
	v_cndmask_b32_e64 v8, 0, 32, vcc
	v_ldexp_f32 v7, v7, v8
	v_log_f32_e32 v7, v7
	v_cndmask_b32_e32 v8, 0, v5, vcc
	v_mul_f32_e32 v9, 0x3f317217, v7
	v_fma_f32 v9, v7, s6, -v9
	v_fmac_f32_e32 v9, 0x3377d1cf, v7
	v_fmac_f32_e32 v9, 0x3f317217, v7
	v_cmp_lt_f32_e64 vcc, |v7|, s7
	s_nop 1
	v_cndmask_b32_e32 v7, v7, v9, vcc
	v_sub_f32_e32 v7, v7, v8
	v_div_scale_f32 v8, s[18:19], s16, s16, v7
	v_rcp_f32_e32 v9, v8
	v_div_scale_f32 v10, vcc, v7, s16, v7
	v_fma_f32 v11, -v8, v9, 1.0
	v_fmac_f32_e32 v9, v11, v9
	v_mul_f32_e32 v11, v10, v9
	v_fma_f32 v12, -v8, v11, v10
	v_fmac_f32_e32 v11, v12, v9
	v_fma_f32 v8, -v8, v11, v10
	v_div_fmas_f32 v8, v8, v9, v11
	v_div_fixup_f32 v7, v8, s16, v7
	v_mul_f32_e32 v7, 0x41800000, v7
	v_cvt_i32_f32_e32 v7, v7
	v_min_i32_e32 v7, 15, v7
	v_add_u32_e32 v7, 16, v7
	s_branch .Lbfb_l1
.Lbfb_l1:
	s_or_b64 exec, exec, s[12:13]
	v_mad_u64_u32 v[8:9], s[12:13], v7, 12, v[2:3]
	v_ashrrev_i32_e32 v9, 31, v8
	v_lshl_add_u64 v[8:9], v[8:9], 2, s[20:21]
	global_load_dword v186, v[8:9], off
	v_mov_b32_e32 v191, 1
.Lbfb_t1:
	s_or_b64 exec, exec, s[10:11]
	v_add_u32_e32 v6, 0x200, v6
	v_add_u32_e32 v4, 0xfffffe00, v4
	v_mov_b32_e32 v192, 0
	v_mul_u32_u24_e32 v2, 0xaaab, v6
	v_lshrrev_b32_e32 v2, 23, v2
	v_mul_i32_i24_e32 v8, 0xffffff40, v2
	v_add3_u32 v7, v8, v6, s3
	v_cmp_lt_u32_e32 vcc, s4, v7
	v_mov_b32_e32 v7, 0xf149f2ca
	s_and_saveexec_b64 s[10:11], vcc
	s_cbranch_execz .Lbfb_t2
	v_sub_u32_e32 v7, v4, v8
	v_lshrrev_b32_e32 v8, 1, v2
	v_and_b32_e32 v8, 14, v8
	v_lshlrev_b32_e32 v7, v8, v7
	v_cmp_lt_u32_e32 vcc, 15, v7
	s_and_saveexec_b64 s[12:13], vcc
	s_cbranch_execz .Lbfb_l2
	v_cvt_f32_u32_e32 v7, v7
	v_mul_f32_e32 v7, 0x3d800000, v7
	v_cmp_gt_f32_e32 vcc, s5, v7
	s_nop 1
	v_cndmask_b32_e64 v8, 0, 32, vcc
	v_ldexp_f32 v7, v7, v8
	v_log_f32_e32 v7, v7
	v_cndmask_b32_e32 v8, 0, v5, vcc
	v_mul_f32_e32 v9, 0x3f317217, v7
	v_fma_f32 v9, v7, s6, -v9
	v_fmac_f32_e32 v9, 0x3377d1cf, v7
	v_fmac_f32_e32 v9, 0x3f317217, v7
	v_cmp_lt_f32_e64 vcc, |v7|, s7
	s_nop 1
	v_cndmask_b32_e32 v7, v7, v9, vcc
	v_sub_f32_e32 v7, v7, v8
	v_div_scale_f32 v8, s[18:19], s16, s16, v7
	v_rcp_f32_e32 v9, v8
	v_div_scale_f32 v10, vcc, v7, s16, v7
	v_fma_f32 v11, -v8, v9, 1.0
	v_fmac_f32_e32 v9, v11, v9
	v_mul_f32_e32 v11, v10, v9
	v_fma_f32 v12, -v8, v11, v10
	v_fmac_f32_e32 v11, v12, v9
	v_fma_f32 v8, -v8, v11, v10
	v_div_fmas_f32 v8, v8, v9, v11
	v_div_fixup_f32 v7, v8, s16, v7
	v_mul_f32_e32 v7, 0x41800000, v7
	v_cvt_i32_f32_e32 v7, v7
	v_min_i32_e32 v7, 15, v7
	v_add_u32_e32 v7, 16, v7
	s_branch .Lbfb_l2
; #define LAS __attribute__((address_space(3)))
; __device__ __forceinline__ void fill_bias_tables(LAS unsigned char* lds, int tid, const float* table, bool dilated) {
;     for (int idx = tid; idx < 12 * BT_FLOATS; idx += NTHREADS) { const int h = idx / BT_FLOATS, j = idx - h * BT_FLOATS, o = 159 - j;
;         const int dil = dilated ? (1 << (2 * (h >> 2))) : 1, maxd = dilated ? 128 : 127; float val = -1e30f;
;         if (o >= 0 && o <= maxd) val = table[t5_bucket(o * dil) * 12 + h] * LOG2E;
;         ((LAS float*)(lds + B_OFF))[idx] = val; }
; }
.Lbfb_l2:
	s_or_b64 exec, exec, s[12:13]
	v_mad_u64_u32 v[8:9], s[12:13], v7, 12, v[2:3]
	v_ashrrev_i32_e32 v9, 31, v8
	v_lshl_add_u64 v[8:9], v[8:9], 2, s[20:21]
	global_load_dword v187, v[8:9], off
	v_mov_b32_e32 v192, 1
.Lbfb_t2:
	s_or_b64 exec, exec, s[10:11]
	v_add_u32_e32 v6, 0x200, v6
	v_add_u32_e32 v4, 0xfffffe00, v4
	v_mov_b32_e32 v193, 0
	v_mul_u32_u24_e32 v2, 0xaaab, v6
	v_lshrrev_b32_e32 v2, 23, v2
	v_mul_i32_i24_e32 v8, 0xffffff40, v2
	v_add3_u32 v7, v8, v6, s3
	v_cmp_lt_u32_e32 vcc, s4, v7
	v_mov_b32_e32 v7, 0xf149f2ca
	s_and_saveexec_b64 s[10:11], vcc
	s_cbranch_execz .Lbfb_t3
	v_sub_u32_e32 v7, v4, v8
	v_lshrrev_b32_e32 v8, 1, v2
	v_and_b32_e32 v8, 14, v8
	v_lshlrev_b32_e32 v7, v8, v7
	v_cmp_lt_u32_e32 vcc, 15, v7
	s_and_saveexec_b64 s[12:13], vcc
	s_cbranch_execz .Lbfb_l3
	v_cvt_f32_u32_e32 v7, v7
	v_mul_f32_e32 v7, 0x3d800000, v7
	v_cmp_gt_f32_e32 vcc, s5, v7
	s_nop 1
	v_cndmask_b32_e64 v8, 0, 32, vcc
	v_ldexp_f32 v7, v7, v8
	v_log_f32_e32 v7, v7
	v_cndmask_b32_e32 v8, 0, v5, vcc
	v_mul_f32_e32 v9, 0x3f317217, v7
	v_fma_f32 v9, v7, s6, -v9
	v_fmac_f32_e32 v9, 0x3377d1cf, v7
	v_fmac_f32_e32 v9, 0x3f317217, v7
	v_cmp_lt_f32_e64 vcc, |v7|, s7
	s_nop 1
	v_cndmask_b32_e32 v7, v7, v9, vcc
	v_sub_f32_e32 v7, v7, v8
	v_div_scale_f32 v8, s[18:19], s16, s16, v7
	v_rcp_f32_e32 v9, v8
	v_div_scale_f32 v10, vcc, v7, s16, v7
	v_fma_f32 v11, -v8, v9, 1.0
	v_fmac_f32_e32 v9, v11, v9
	v_mul_f32_e32 v11, v10, v9
	v_fma_f32 v12, -v8, v11, v10
	v_fmac_f32_e32 v11, v12, v9
	v_fma_f32 v8, -v8, v11, v10
	v_div_fmas_f32 v8, v8, v9, v11
	v_div_fixup_f32 v7, v8, s16, v7
	v_mul_f32_e32 v7, 0x41800000, v7
	v_cvt_i32_f32_e32 v7, v7
	v_min_i32_e32 v7, 15, v7
	v_add_u32_e32 v7, 16, v7
	s_branch .Lbfb_l3
.Lbfb_l3:
	s_or_b64 exec, exec, s[12:13]
	v_mad_u64_u32 v[8:9], s[12:13], v7, 12, v[2:3]
	v_ashrrev_i32_e32 v9, 31, v8
	v_lshl_add_u64 v[8:9], v[8:9], 2, s[20:21]
	global_load_dword v188, v[8:9], off
	v_mov_b32_e32 v193, 1
.Lbfb_t3:
	s_or_b64 exec, exec, s[10:11]
	v_add_u32_e32 v6, 0x200, v6
	v_add_u32_e32 v4, 0xfffffe00, v4
	v_cmp_gt_u32_e32 vcc, 0x900, v6
	s_and_saveexec_b64 s[8:9], vcc
	s_cbranch_execz .Lbfb_skip4
	v_mov_b32_e32 v194, 0
	v_mul_u32_u24_e32 v2, 0xaaab, v6
	v_lshrrev_b32_e32 v2, 23, v2
	v_mul_i32_i24_e32 v8, 0xffffff40, v2
	v_add3_u32 v7, v8, v6, s3
	v_cmp_lt_u32_e32 vcc, s4, v7
	v_mov_b32_e32 v7, 0xf149f2ca
	s_and_saveexec_b64 s[10:11], vcc
	s_cbranch_execz .Lbfb_t4
	v_sub_u32_e32 v7, v4, v8
	v_lshrrev_b32_e32 v8, 1, v2
	v_and_b32_e32 v8, 14, v8
	v_lshlrev_b32_e32 v7, v8, v7
	v_cmp_lt_u32_e32 vcc, 15, v7
	s_and_saveexec_b64 s[12:13], vcc
	s_cbranch_execz .Lbfb_l4
	v_cvt_f32_u32_e32 v7, v7
	v_mul_f32_e32 v7, 0x3d800000, v7
	v_cmp_gt_f32_e32 vcc, s5, v7
	s_nop 1
	v_cndmask_b32_e64 v8, 0, 32, vcc
	v_ldexp_f32 v7, v7, v8
	v_log_f32_e32 v7, v7
	v_cndmask_b32_e32 v8, 0, v5, vcc
	v_mul_f32_e32 v9, 0x3f317217, v7
	v_fma_f32 v9, v7, s6, -v9
	v_fmac_f32_e32 v9, 0x3377d1cf, v7
	v_fmac_f32_e32 v9, 0x3f317217, v7
	v_cmp_lt_f32_e64 vcc, |v7|, s7
	s_nop 1
	v_cndmask_b32_e32 v7, v7, v9, vcc
	v_sub_f32_e32 v7, v7, v8
	v_div_scale_f32 v8, s[18:19], s16, s16, v7
	v_rcp_f32_e32 v9, v8
	v_div_scale_f32 v10, vcc, v7, s16, v7
	v_fma_f32 v11, -v8, v9, 1.0
	v_fmac_f32_e32 v9, v11, v9
	v_mul_f32_e32 v11, v10, v9
	v_fma_f32 v12, -v8, v11, v10
	v_fmac_f32_e32 v11, v12, v9
	v_fma_f32 v8, -v8, v11, v10
	v_div_fmas_f32 v8, v8, v9, v11
	v_div_fixup_f32 v7, v8, s16, v7
	v_mul_f32_e32 v7, 0x41800000, v7
	v_cvt_i32_f32_e32 v7, v7
	v_min_i32_e32 v7, 15, v7
	v_add_u32_e32 v7, 16, v7
	s_branch .Lbfb_l4
.Lbfb_l4:
	s_or_b64 exec, exec, s[12:13]
	v_mad_u64_u32 v[8:9], s[12:13], v7, 12, v[2:3]
	v_ashrrev_i32_e32 v9, 31, v8
	v_lshl_add_u64 v[8:9], v[8:9], 2, s[20:21]
	global_load_dword v189, v[8:9], off
	v_mov_b32_e32 v194, 1
.Lbfb_t4:
	s_or_b64 exec, exec, s[10:11]
	v_add_u32_e32 v6, 0x200, v6
	v_add_u32_e32 v4, 0xfffffe00, v4
